# layer-0 attention phase: convert-last workgroups now run dense -> convert -> sparse, so the weight stream never runs beside a sparse-attention pass (K/V DMA latency bound) of either workgroup half
# speedup vs baseline: 1.0061x; 1.0061x over previous
; #define LAS __attribute__((address_space(3)))
; __global__ void __launch_bounds__(NTHR, 2) fwd(Params p) {
;     extern __shared__ __attribute__((aligned(16))) unsigned char lds_raw[];
;     LAS unsigned char* lds = (LAS unsigned char*)lds_raw;
;     const int tid0 = threadIdx.x, bid = blockIdx.x, G = gridDim.x;
;     const int wv = __builtin_amdgcn_readfirstlane(tid0 >> 6);
;     const int vcu = (G % 8 == 0) ? (bid % 8) * (G / 8) + bid / 8 : bid;
;     unsigned* ctl = (unsigned*)(p.ws + WS_CTL);
;     if (tid0 < 4) ((LAS unsigned*)(lds + MISC_OFF))[tid0] = 0u;
;     __syncthreads();
;     XcdBarrier bar; bar.bar = ctl + CW_BAR; bar.x = 0; bar.st = (volatile LAS unsigned*)(lds + MISC_OFF);
;     if (N_LAUNCH_MODE == 1) bar = xcd_barrier_post(ctl + CW_BAR, (volatile LAS unsigned*)(lds + MISC_OFF));
_Z3fwd6Params:
	s_mov_b64 s[76:77], s[0:1]
	s_mov_b32 s100, 0
	s_mov_b32 s101, 0
	s_nop 0
	v_writelane_b32 v255, s100, 63
	s_load_dword s50, s[0:1], 0xf8
	s_nop 0
	s_load_dwordx2 s[0:1], s[0:1], 0xe8
	s_mov_b32 s30, s2
	s_add_u32 s2, s76, 0xf8
	s_addc_u32 s3, s77, 0
	v_readfirstlane_b32 s8, v0
	v_writelane_b32 v252, s2, 0
	s_nop 1
	v_writelane_b32 v252, s3, 1
	s_waitcnt lgkmcnt(0)
	s_and_b32 s2, s50, 7
	s_cmp_lg_u32 s2, 0
	s_mov_b32 s2, s30
	v_writelane_b32 v252, s2, 2
	s_cbranch_scc1 .LBB0_1
	s_getpc_b64 s[98:99]

; #define LAS __attribute__((address_space(3)))
; __device__ __forceinline__ int fresh_tid(int wv) { int l; asm volatile("v_mbcnt_lo_u32_b32 %0, -1, 0\n\tv_mbcnt_hi_u32_b32 %0, -1, %0" : "=v"(l)); return wv * 64 + l; }
; __global__ void __launch_bounds__(NTHR, 2) fwd(Params p) {
;     ...
;                 __syncthreads();
;                 if (ATT_ONLY < 0 || ATT_ONLY == 2)
;                 _Pragma("unroll 1") for (int rep = 0; rep < NREPA(2); ++rep)
;                 for (int it = vcu; it < 1024; it += G) {
;                     const int tid2 = fresh_tid(wv), wid = __builtin_amdgcn_readfirstlane(tid2 >> 6), lane = tid2 & 63;
;                     const int w = it * 8 + wid; LAS unsigned char* wl = lds + wid * da::SP_WAVE_LDS;
;                     if constexpr (F8_SPARSE) { const unsigned char* ra8 = (const unsigned char*)RA; PolB8 pol; pol.init(Hx, Oat, ra8, ra8 + 32 * MiB, ra8 + 64 * MiB, ra8 + 96 * MiB, w, lane); d8::sparse8_wave(pol, wl, lane); }
;                     else { PolB pol; pol.init(Hx, Oat, w, lane); da::sparse_wave(pol, wl, lane); }
;                 }
;     ...
;             if (CONV_BESIDE && L == 0 && !conv_first) { __syncthreads(); phase_prologue(ka, ws, lds, G, bid, fresh_tid(wv), 2, 12, false); }
.LBB0_541:
	v_readlane_b32 s0, v255, 63
	v_readlane_b32 s1, v253, 18
	v_readlane_b32 s2, v255, 53
	s_nop 0
	s_or_b32 s0, s0, s1
	s_or_b32 s0, s0, s2
	s_cmp_lg_u32 s0, 0
	s_cbranch_scc1 .Lcmid_no
	s_mov_b32 s0, 1
	v_writelane_b32 v255, s0, 63
	s_branch .LBB0_580
.Lcmid_back:
	v_readlane_b32 s0, v253, 24
	v_readlane_b32 s1, v253, 25
	v_readlane_b32 s2, v255, 57
	v_readlane_b32 s3, v255, 58
	s_nop 0
	s_load_dwordx2 s[6:7], s[2:3], 0xe0
	v_cndmask_b32_e64 v0, 0, 1, s[0:1]
	v_cmp_ne_u32_e64 s[38:39], 1, v0
	s_add_u32 s68, s46, 0x24600000
	s_addc_u32 s69, s47, 0
	s_add_u32 s2, s46, 0x36600000
	s_addc_u32 s3, s47, 0
	v_readlane_b32 s0, v255, 51
	v_readlane_b32 s1, v255, 52
	s_waitcnt lgkmcnt(0)
	s_add_u32 s6, s6, 0x6000000
	s_addc_u32 s7, s7, 0
	s_and_b64 s[0:1], s[0:1], exec
	s_cselect_b32 s71, s3, s7
	s_cselect_b32 s70, s2, s6

; __device__ __forceinline__ void phase_prologue(kcu64_t* ka, unsigned char* ws, LAS unsigned char* lds, int G, int bid, int tid, int jlo, int jhi, bool do_x) {
;     LAS unsigned* tl = (LAS unsigned*)lds;
;     constexpr int NJ = 12;
;     const int cnts[NJ] = {16 * 72, 16 * 32, 4096, 4096, 4096, 16 * 61, 16 * 32, 4096, 4096, 4096, 4 * 24, 2 * 32};
;     int t_lo = 0, t_hi = 0;
; #pragma unroll
;     for (int j = 0; j < NJ; ++j) { if (j < jlo) t_lo += cnts[j]; if (j < jhi) t_hi += cnts[j]; }
;     for (int t = t_lo + bid; t < t_hi; t += G) {
;         int j = 0, base = 0;
; #pragma unroll
;         for (int q = 0; q < NJ - 1; ++q) if (t >= base + cnts[q] && j == q) { base += cnts[q]; j = q + 1; }
;         const int tt = t - base;
;         TJob jb;
;         switch (j) {
;             case 0: jb = TJob{PIN(I_WIN0), (bf16_t*)(ws + WS_WIN0), nullptr, 2048, IN0, 2048, 0, 0, 0, F8_IN}; break;
;             case 1: jb = TJob{PIN(I_WOUT0), (bf16_t*)(ws + WS_WOUT0), nullptr, 2048, 2048, 2048, 0, 0, 0, F8_OUT}; break;
;             case 2: jb = TJob{PIN(I_WG0), (bf16_t*)(ws + WS_WGU0), nullptr, 2048, 512, 2048, 1, (size_t)2048 * 512, (size_t)1024 * 2048, F8_GU}; break;
;             case 3: jb = TJob{PIN(I_WU0), (bf16_t*)(ws + WS_WGU0), nullptr, 2048, 512, 2048, 2, (size_t)2048 * 512, (size_t)1024 * 2048, F8_GU}; break;
;             case 4: jb = TJob{PIN(I_WD0), (bf16_t*)(ws + WS_WD0), nullptr, 512, 2048, 512, 0, (size_t)512 * 2048, (size_t)2048 * 512, F8_DOWN}; break;
;             case 5: jb = TJob{PIN(I_WIN1), (bf16_t*)(ws + WS_WIN1), nullptr, 2048, IN1, 2048, 0, 0, 0, F8_IN}; break;
;             case 6: jb = TJob{PIN(I_WOUT1), (bf16_t*)(ws + WS_WOUT1), nullptr, 2048, 2048, 2048, 0, 0, 0, F8_OUT}; break;
;             case 7: jb = TJob{PIN(I_WG1), (bf16_t*)(ws + WS_WGU1), nullptr, 2048, 512, 2048, 1, (size_t)2048 * 512, (size_t)1024 * 2048, F8_GU}; break;
;             case 8: jb = TJob{PIN(I_WU1), (bf16_t*)(ws + WS_WGU1), nullptr, 2048, 512, 2048, 2, (size_t)2048 * 512, (size_t)1024 * 2048, F8_GU}; break;
;             case 9: jb = TJob{PIN(I_WD1), (bf16_t*)(ws + WS_WD1), nullptr, 512, 2048, 512, 0, (size_t)512 * 2048, (size_t)2048 * 512, F8_DOWN}; break;
; __global__ void __launch_bounds__(NTHR, 2) fwd(Params p) {
;     ...
;             if (CONV_BESIDE && L == 0 && !conv_first) { __syncthreads(); phase_prologue(ka, ws, lds, G, bid, fresh_tid(wv), 2, 12, false); }
.LBB0_580:
	v_readlane_b32 s0, v253, 18
	v_readlane_b32 s33, v255, 53
	s_or_b32 s0, s33, s0
	v_readlane_b32 s1, v255, 63
	s_nop 0
	s_lshr_b32 s1, s1, 1
	s_or_b32 s0, s0, s1
	s_cmp_lg_u32 s0, 0
	v_readlane_b32 s80, v255, 50
	s_mov_b32 s82, 0x5010400
	s_cbranch_scc1 .LBB0_633
	v_readlane_b32 s0, v253, 21
	v_readlane_b32 s1, v253, 22
	s_waitcnt vmcnt(0) lgkmcnt(0)
	s_barrier
	v_mbcnt_lo_u32_b32 v0, -1, 0
	v_mbcnt_hi_u32_b32 v0, -1, v0
	s_andn2_b64 vcc, exec, s[0:1]
	v_add_u32_e32 v16, s5, v0
	s_cbranch_vccnz .LBB0_629
	v_readlane_b32 s2, v255, 57
	v_readlane_b32 s3, v255, 58
	s_add_u32 s0, s2, 0x88
	s_addc_u32 s1, s3, 0
	v_writelane_b32 v255, s0, 59
	v_lshlrev_b32_e32 v1, 2, v0
	v_and_b32_e32 v2, 60, v1
	v_writelane_b32 v255, s1, 60
	s_add_u32 s0, s46, 0x1c200000
	s_addc_u32 s1, s47, 0
	s_add_u32 s34, s2, 0xc8
	s_addc_u32 s35, s3, 0
	s_add_u32 s38, s46, 0x18200000
	s_addc_u32 s39, s47, 0
	s_add_u32 s40, s2, 0xc0
	s_addc_u32 s41, s3, 0
	s_add_u32 s42, s46, 0x10200000
	s_addc_u32 s43, s47, 0
	s_add_u32 s44, s2, 0xb8
	s_addc_u32 s45, s3, 0
	s_add_u32 s68, s2, 0xa0
	s_addc_u32 s69, s3, 0
	s_add_u32 s70, s46, 0xfa00000
	s_addc_u32 s71, s47, 0
	s_add_u32 s72, s2, 0x70
	s_addc_u32 s73, s3, 0
	s_add_u32 s74, s46, 0xea00000
	s_addc_u32 s75, s47, 0
	s_add_u32 s76, s2, 0x58
	s_addc_u32 s77, s3, 0
	s_add_u32 s78, s46, 0xaa00000
	s_addc_u32 s79, s47, 0
	s_add_u32 s84, s2, 0x50
	s_addc_u32 s85, s3, 0
	s_add_u32 s92, s46, 0x2a00000
	s_addc_u32 s93, s47, 0
	s_add_u32 s96, s2, 0x48
	v_writelane_b32 v255, s0, 61
	s_addc_u32 s97, s3, 0
	v_ashrrev_i32_e32 v1, 4, v16
	v_writelane_b32 v255, s1, 62
	s_add_u32 s0, s2, 48
	s_addc_u32 s1, s3, 0
	s_add_u32 s94, s46, 0x2200000
	s_addc_u32 s95, s47, 0
	s_add_u32 s6, s2, 24
	s_addc_u32 s7, s3, 0
	s_add_u32 s52, s46, 0x1000000
	s_addc_u32 s53, s47, 0
	s_add_u32 s18, s2, 0x98
	v_ashrrev_i32_e32 v24, 3, v16
	s_movk_i32 s8, 0x84
	s_addc_u32 s19, s3, 0
	v_lshlrev_b32_e32 v17, 2, v1
	v_mul_lo_u32 v4, v24, s8
	v_lshlrev_b32_e32 v0, 4, v0
	s_add_u32 s2, s46, 0x1c400000
	v_add_u32_e32 v1, 0, v17
	v_mul_u32_u24_e32 v3, 0x84, v2
	v_add_u32_e32 v4, 0, v4
	v_and_b32_e32 v18, 0x70, v0
	s_addc_u32 s3, s47, 0
	v_mov_b32_e32 v19, v233
	v_lshlrev_b32_e32 v232, 2, v2
	v_add_u32_e32 v25, v1, v3
	v_add_u32_e32 v26, v4, v18
	v_readlane_b32 s15, v253, 23
	s_branch .LBB0_589

; __device__ __forceinline__ int fresh_tid(int wv) { int l; asm volatile("v_mbcnt_lo_u32_b32 %0, -1, 0\n\tv_mbcnt_hi_u32_b32 %0, -1, %0" : "=v"(l)); return wv * 64 + l; }
; __global__ void __launch_bounds__(NTHR, 2) fwd(Params p) {
;     ...
;             if (CONV_BESIDE && L == 0 && !conv_first) { __syncthreads(); phase_prologue(ka, ws, lds, G, bid, fresh_tid(wv), 2, 12, false); }
.LBB0_633:
	v_readlane_b32 s0, v255, 63
	s_nop 0
	s_cmp_eq_u32 s0, 1
	s_cbranch_scc0 .Lcmid_end
	s_mov_b32 s0, 2
	v_writelane_b32 v255, s0, 63
	s_branch .Lcmid_back
